# P0: once-read streams (w_in transposer loads, x rows) with nt cache policy
# speedup vs baseline: 1.0149x; 1.0149x over previous
; template <int FP8> __device__ __forceinline__ void transpose_stream(const float* W, int K, int N, void* WT_, int split, int add, int ldt, int col_add, LAS float* scr, int it0, int its, int nitems, int lane, const float* kscale) {
;     const int nblk = N / 32; float cur[32];
;     if (it0 < nitems) { const int kb = it0 / nblk, nb = it0 % nblk;
; #pragma unroll
;         for (int i = 0; i < 32; ++i) cur[i] = W[(size_t)(64 * kb + 2 * i + (lane >> 5)) * N + 32 * nb + (lane & 31)]; }
; __device__ __forceinline__ void p0_prologue(Frame& F) {
;     ...
;     const float* w_in = F.in[2];
;     constexpr int I_IN = (D_ / 64) * (IN_COLS / 32);
;     transpose_stream<2>(w_in, D_, IN_COLS, F.ws + WS_WINT8, RWKV_COLS, 128, 0, 0, scr, F.gw, F.NGW, I_IN, F.lane, nullptr);
.LBB0_7:
	s_load_dwordx16 s[4:19], s[0:1], 0x40
	s_lshr_b32 s66, s70, 6
	s_lshl_b32 s34, s76, 3
	s_waitcnt lgkmcnt(0)
	v_writelane_b32 v254, s4, 2
	s_nop 1
	v_writelane_b32 v254, s5, 3
	v_writelane_b32 v254, s6, 4
	v_writelane_b32 v254, s7, 5
	v_writelane_b32 v254, s8, 6
	v_writelane_b32 v254, s9, 7
	v_writelane_b32 v254, s10, 8
	v_writelane_b32 v254, s11, 9
	v_writelane_b32 v254, s12, 10
	v_writelane_b32 v254, s13, 11
	v_writelane_b32 v254, s14, 12
	v_writelane_b32 v254, s15, 13
	v_writelane_b32 v254, s16, 14
	v_writelane_b32 v254, s17, 15
	v_writelane_b32 v254, s18, 16
	v_writelane_b32 v254, s19, 17
	s_load_dwordx16 s[12:27], s[0:1], 0x80
	s_lshl_b32 s0, s2, 3
	s_add_i32 s94, s66, s0
	s_cmp_gt_i32 s84, 0
	s_cselect_b64 s[0:1], -1, 0
	s_cmp_lt_i32 s85, 1
	s_cselect_b64 s[4:5], -1, 0
	s_or_b64 s[0:1], s[0:1], s[4:5]
	s_and_b64 vcc, exec, s[0:1]
	s_cbranch_vccnz .LBB0_101
	s_lshl_b32 s0, s66, 14
	v_mbcnt_lo_u32_b32 v6, -1, 0
	v_mbcnt_hi_u32_b32 v6, -1, v6
	s_add_i32 s28, s0, 0
	v_ashrrev_i32_e32 v1, 5, v6
	v_and_b32_e32 v2, 31, v6
	s_movk_i32 s0, 0x84
	v_lshlrev_b32_e32 v10, 2, v2
	v_mul_lo_u32 v2, v1, s0
	s_mov_b32 s3, 0
	s_cmp_gt_i32 s94, 0xa2ff
	v_mov_b32_e32 v11, 0
	v_add3_u32 v7, s28, v10, v2
	s_cbranch_scc1 .LBB0_15
	s_mul_hi_i32 s0, s94, 0xc907da5
	s_lshr_b32 s1, s0, 31
	s_ashr_i32 s0, s0, 5
	s_add_i32 s4, s0, s1
	s_mul_i32 s0, s4, 0x28c
	s_sub_i32 s0, s94, s0
	s_lshl_b32 s0, s0, 5
	s_ashr_i32 s1, s0, 31
	s_lshl_b64 s[0:1], s[0:1], 2
	s_add_u32 s0, s40, s0
	s_addc_u32 s1, s41, s1
	v_lshl_add_u32 v64, s4, 6, v1
	v_lshl_add_u64 v[2:3], s[0:1], 0, v[10:11]
	s_mov_b32 s6, 0x14600
	v_add_u32_e32 v56, 14, v64
	v_add_u32_e32 v58, 10, v64
	v_add_u32_e32 v62, 4, v64
	v_add_u32_e32 v4, 62, v64
	v_add_u32_e32 v8, 60, v64
	v_add_u32_e32 v12, 58, v64
	v_add_u32_e32 v14, 56, v64
	v_add_u32_e32 v16, 54, v64
	v_add_u32_e32 v18, 52, v64
	v_add_u32_e32 v20, 50, v64
	v_add_u32_e32 v22, 48, v64
	v_add_u32_e32 v24, 46, v64
	v_add_u32_e32 v26, 44, v64
	v_add_u32_e32 v28, 42, v64
	v_add_u32_e32 v30, 40, v64
	v_add_u32_e32 v32, 38, v64
	v_add_u32_e32 v34, 36, v64
	v_add_u32_e32 v36, 34, v64
	v_add_u32_e32 v38, 32, v64
	v_add_u32_e32 v40, 30, v64
	v_add_u32_e32 v42, 28, v64
	v_add_u32_e32 v44, 26, v64
	v_add_u32_e32 v46, 24, v64
	v_add_u32_e32 v48, 22, v64
	v_add_u32_e32 v50, 20, v64
	v_add_u32_e32 v52, 18, v64
	v_add_u32_e32 v54, 16, v64
	v_mad_i64_i32 v[66:67], s[0:1], v56, s6, v[2:3]
	v_add_u32_e32 v56, 12, v64
	v_mad_i64_i32 v[68:69], s[0:1], v58, s6, v[2:3]
	v_add_u32_e32 v58, 8, v64
	v_add_u32_e32 v60, 6, v64
	v_mad_i64_i32 v[70:71], s[0:1], v62, s6, v[2:3]
	v_add_u32_e32 v62, 2, v64
	v_mad_i64_i32 v[4:5], s[0:1], v4, s6, v[2:3]
	v_mad_i64_i32 v[8:9], s[0:1], v8, s6, v[2:3]
	v_mad_i64_i32 v[12:13], s[0:1], v12, s6, v[2:3]
	v_mad_i64_i32 v[14:15], s[0:1], v14, s6, v[2:3]
	v_mad_i64_i32 v[16:17], s[0:1], v16, s6, v[2:3]
	v_mad_i64_i32 v[18:19], s[0:1], v18, s6, v[2:3]
	v_mad_i64_i32 v[20:21], s[0:1], v20, s6, v[2:3]
	v_mad_i64_i32 v[22:23], s[0:1], v22, s6, v[2:3]
	v_mad_i64_i32 v[24:25], s[0:1], v24, s6, v[2:3]
	v_mad_i64_i32 v[26:27], s[0:1], v26, s6, v[2:3]
	v_mad_i64_i32 v[28:29], s[0:1], v28, s6, v[2:3]
	v_mad_i64_i32 v[30:31], s[0:1], v30, s6, v[2:3]
	v_mad_i64_i32 v[32:33], s[0:1], v32, s6, v[2:3]
	v_mad_i64_i32 v[34:35], s[0:1], v34, s6, v[2:3]
	v_mad_i64_i32 v[36:37], s[0:1], v36, s6, v[2:3]
	v_mad_i64_i32 v[38:39], s[0:1], v38, s6, v[2:3]
	v_mad_i64_i32 v[40:41], s[0:1], v40, s6, v[2:3]
	v_mad_i64_i32 v[42:43], s[0:1], v42, s6, v[2:3]
	v_mad_i64_i32 v[44:45], s[0:1], v44, s6, v[2:3]
	v_mad_i64_i32 v[46:47], s[0:1], v46, s6, v[2:3]
	v_mad_i64_i32 v[48:49], s[0:1], v48, s6, v[2:3]
	v_mad_i64_i32 v[50:51], s[0:1], v50, s6, v[2:3]
	v_mad_i64_i32 v[52:53], s[0:1], v52, s6, v[2:3]
	v_mad_i64_i32 v[54:55], s[0:1], v54, s6, v[2:3]
	v_mad_i64_i32 v[56:57], s[0:1], v56, s6, v[2:3]
	v_mad_i64_i32 v[58:59], s[0:1], v58, s6, v[2:3]
	v_mad_i64_i32 v[60:61], s[0:1], v60, s6, v[2:3]
	v_mad_i64_i32 v[62:63], s[0:1], v62, s6, v[2:3]
	v_mad_i64_i32 v[2:3], s[0:1], v64, s6, v[2:3]
	global_load_dword v64, v[2:3], off nt
	s_nop 0
	global_load_dword v63, v[62:63], off nt
	s_nop 0
	global_load_dword v62, v[70:71], off nt
	s_nop 0
	global_load_dword v61, v[60:61], off nt
	s_nop 0
	global_load_dword v59, v[58:59], off nt
	s_nop 0
	global_load_dword v58, v[68:69], off nt
	s_nop 0
	global_load_dword v57, v[56:57], off nt
	s_nop 0
	global_load_dword v56, v[66:67], off nt
	s_nop 0
	global_load_dword v54, v[54:55], off nt
	s_nop 0
	global_load_dword v53, v[52:53], off nt
	s_nop 0
	global_load_dword v52, v[50:51], off nt
	s_nop 0
	global_load_dword v51, v[48:49], off nt
	s_nop 0
	global_load_dword v49, v[46:47], off nt
	global_load_dword v48, v[44:45], off nt
	s_nop 0
	global_load_dword v47, v[42:43], off nt
	global_load_dword v46, v[40:41], off nt
	global_load_dword v44, v[38:39], off nt
	s_nop 0
	global_load_dword v43, v[36:37], off nt
	global_load_dword v42, v[34:35], off nt
	global_load_dword v41, v[32:33], off nt
	global_load_dword v39, v[30:31], off nt
	global_load_dword v38, v[28:29], off nt
	s_nop 0
	global_load_dword v37, v[26:27], off nt
	global_load_dword v36, v[24:25], off nt
	global_load_dword v35, v[22:23], off nt
	global_load_dword v34, v[20:21], off nt
	global_load_dword v33, v[18:19], off nt
	global_load_dword v32, v[16:17], off nt
	global_load_dword v31, v[14:15], off nt
	global_load_dword v30, v[12:13], off nt
	global_load_dword v29, v[8:9], off nt
	global_load_dword v28, v[4:5], off nt
	v_lshlrev_b32_e32 v4, 4, v6
	v_and_b32_e32 v4, 48, v4
	v_mov_b32_e32 v5, v11
	v_lshl_add_u64 v[2:3], s[40:41], 0, v[10:11]
	v_mul_u32_u24_e32 v9, 0x84, v4
	v_lshl_add_u64 v[4:5], s[68:69], 0, v[4:5]
	s_mov_b64 s[0:1], 0x17000000
	v_and_b32_e32 v11, -4, v6
	v_ashrrev_i32_e32 v8, 2, v6
	v_lshl_add_u64 v[4:5], v[4:5], 0, s[0:1]
	v_add3_u32 v9, s28, v9, v11
	s_lshl_b32 s11, s94, 5
	s_lshl_b32 s7, s34, 5
	s_mov_b32 s8, 0xc2fe0000
	s_mov_b32 s9, 0xc0c0500
	v_mov_b32_e32 v11, 0x42fe0000
	s_mov_b32 s30, s94
	s_branch .LBB0_11

; template <int FP8> __device__ __forceinline__ void transpose_stream(const float* W, int K, int N, void* WT_, int split, int add, int ldt, int col_add, LAS float* scr, int it0, int its, int nitems, int lane, const float* kscale) {
;     ...
;     for (int it = it0; it < nitems; it += its) {
;         float nxt[32]; const int itn = it + its;
;         if (itn < nitems) { const int kb = itn / nblk, nb = itn % nblk;
; #pragma unroll
;             for (int i = 0; i < 32; ++i) nxt[i] = W[(size_t)(64 * kb + 2 * i + (lane >> 5)) * N + 32 * nb + (lane & 31)]; }
;         else {
; #pragma unroll
;             for (int i = 0; i < 32; ++i) nxt[i] = 0.f; }
.LBB0_13:
	v_mov_b32_e32 v12, 0
	s_andn2_b64 vcc, exec, s[4:5]
	v_mov_b32_e32 v13, 0
	v_mov_b32_e32 v14, 0
	v_mov_b32_e32 v15, 0
	v_mov_b32_e32 v16, 0
	v_mov_b32_e32 v17, 0
	v_mov_b32_e32 v18, 0
	v_mov_b32_e32 v19, 0
	v_mov_b32_e32 v20, 0
	v_mov_b32_e32 v21, 0
	v_mov_b32_e32 v22, 0
	v_mov_b32_e32 v23, 0
	v_mov_b32_e32 v24, 0
	v_mov_b32_e32 v25, 0
	v_mov_b32_e32 v26, 0
	v_mov_b32_e32 v27, 0
	v_mov_b32_e32 v40, 0
	v_mov_b32_e32 v45, 0
	v_mov_b32_e32 v50, 0
	v_mov_b32_e32 v55, 0
	v_mov_b32_e32 v60, 0
	v_mov_b32_e32 v65, 0
	v_mov_b32_e32 v66, 0
	v_mov_b32_e32 v67, 0
	v_mov_b32_e32 v68, 0
	v_mov_b32_e32 v69, 0
	v_mov_b32_e32 v70, 0
	v_mov_b32_e32 v71, 0
	v_mov_b32_e32 v72, 0
	v_mov_b32_e32 v73, 0
	v_mov_b32_e32 v74, 0
	v_mov_b32_e32 v75, 0
	s_cbranch_vccnz .LBB0_10
	s_mul_hi_i32 s4, s10, 0xc907da5
	s_lshr_b32 s5, s4, 31
	s_ashr_i32 s4, s4, 5
	s_add_i32 s4, s4, s5
	v_lshl_add_u32 v84, s4, 6, v1
	s_mulk_i32 s4, 0xae80
	s_add_i32 s29, s7, s11
	s_add_i32 s4, s29, s4
	s_ashr_i32 s5, s4, 31
	v_lshl_add_u64 v[68:69], s[4:5], 2, v[2:3]
	v_add_u32_e32 v40, 24, v84
	v_add_u32_e32 v14, 2, v84
	v_add_u32_e32 v16, 4, v84
	v_add_u32_e32 v18, 6, v84
	v_add_u32_e32 v20, 8, v84
	v_add_u32_e32 v22, 10, v84
	v_add_u32_e32 v24, 12, v84
	v_add_u32_e32 v26, 14, v84
	v_mad_i64_i32 v[66:67], s[4:5], v40, s6, v[68:69]
	v_add_u32_e32 v40, 26, v84
	v_mad_i64_i32 v[12:13], s[4:5], v84, s6, v[68:69]
	v_mad_i64_i32 v[14:15], s[4:5], v14, s6, v[68:69]
	v_mad_i64_i32 v[16:17], s[4:5], v16, s6, v[68:69]
	v_mad_i64_i32 v[18:19], s[4:5], v18, s6, v[68:69]
	v_mad_i64_i32 v[20:21], s[4:5], v20, s6, v[68:69]
	v_mad_i64_i32 v[22:23], s[4:5], v22, s6, v[68:69]
	v_mad_i64_i32 v[24:25], s[4:5], v24, s6, v[68:69]
	v_mad_i64_i32 v[26:27], s[4:5], v26, s6, v[68:69]
	v_mad_i64_i32 v[70:71], s[4:5], v40, s6, v[68:69]
	v_add_u32_e32 v40, 28, v84
	global_load_dword v12, v[12:13], off nt
	s_nop 0
	global_load_dword v13, v[14:15], off nt
	s_nop 0
	global_load_dword v14, v[16:17], off nt
	global_load_dword v15, v[18:19], off nt
	s_nop 0
	global_load_dword v16, v[20:21], off nt
	global_load_dword v17, v[22:23], off nt
	global_load_dword v18, v[24:25], off nt
	global_load_dword v19, v[26:27], off nt
	v_add_u32_e32 v20, 16, v84
	v_add_u32_e32 v22, 18, v84
	v_add_u32_e32 v24, 20, v84
	v_add_u32_e32 v26, 22, v84
	v_mad_i64_i32 v[72:73], s[4:5], v40, s6, v[68:69]
	v_add_u32_e32 v40, 30, v84
	v_mad_i64_i32 v[20:21], s[4:5], v20, s6, v[68:69]
	v_mad_i64_i32 v[22:23], s[4:5], v22, s6, v[68:69]
	v_mad_i64_i32 v[24:25], s[4:5], v24, s6, v[68:69]
	v_mad_i64_i32 v[26:27], s[4:5], v26, s6, v[68:69]
	v_mad_i64_i32 v[74:75], s[4:5], v40, s6, v[68:69]
	v_add_u32_e32 v40, 32, v84
	global_load_dword v20, v[20:21], off nt
	s_nop 0
	global_load_dword v21, v[22:23], off nt
	s_nop 0
	global_load_dword v22, v[24:25], off nt
	global_load_dword v23, v[26:27], off nt
	s_nop 0
	global_load_dword v24, v[66:67], off nt
	global_load_dword v25, v[70:71], off nt
	global_load_dword v26, v[72:73], off nt
	global_load_dword v27, v[74:75], off nt
	v_mad_i64_i32 v[66:67], s[4:5], v40, s6, v[68:69]
	v_add_u32_e32 v40, 34, v84
	v_mad_i64_i32 v[70:71], s[4:5], v40, s6, v[68:69]
	v_add_u32_e32 v40, 36, v84
	v_mad_i64_i32 v[72:73], s[4:5], v40, s6, v[68:69]
	v_add_u32_e32 v40, 38, v84
	v_mad_i64_i32 v[74:75], s[4:5], v40, s6, v[68:69]
	v_add_u32_e32 v40, 40, v84
	v_mad_i64_i32 v[76:77], s[4:5], v40, s6, v[68:69]
	v_add_u32_e32 v40, 42, v84
	v_mad_i64_i32 v[78:79], s[4:5], v40, s6, v[68:69]
	v_add_u32_e32 v40, 44, v84
	v_mad_i64_i32 v[80:81], s[4:5], v40, s6, v[68:69]
	v_add_u32_e32 v40, 46, v84
	v_mad_i64_i32 v[82:83], s[4:5], v40, s6, v[68:69]
	global_load_dword v40, v[66:67], off nt
	global_load_dword v45, v[70:71], off nt
	global_load_dword v50, v[72:73], off nt
	global_load_dword v55, v[74:75], off nt
	global_load_dword v60, v[76:77], off nt
	global_load_dword v65, v[78:79], off nt
	global_load_dword v66, v[80:81], off nt
	global_load_dword v67, v[82:83], off nt
	v_add_u32_e32 v70, 48, v84
	v_add_u32_e32 v72, 50, v84
	v_add_u32_e32 v74, 52, v84
	v_mad_i64_i32 v[70:71], s[4:5], v70, s6, v[68:69]
	v_mad_i64_i32 v[72:73], s[4:5], v72, s6, v[68:69]
	v_mad_i64_i32 v[74:75], s[4:5], v74, s6, v[68:69]
	v_add_u32_e32 v76, 54, v84
	v_add_u32_e32 v78, 56, v84
	v_add_u32_e32 v80, 58, v84
	v_add_u32_e32 v82, 60, v84
	v_add_u32_e32 v84, 62, v84
	v_mad_i64_i32 v[76:77], s[4:5], v76, s6, v[68:69]
	v_mad_i64_i32 v[78:79], s[4:5], v78, s6, v[68:69]
	v_mad_i64_i32 v[80:81], s[4:5], v80, s6, v[68:69]
	v_mad_i64_i32 v[82:83], s[4:5], v82, s6, v[68:69]
	v_mad_i64_i32 v[84:85], s[4:5], v84, s6, v[68:69]
	global_load_dword v68, v[70:71], off nt
	global_load_dword v69, v[72:73], off nt
	s_nop 0
	global_load_dword v70, v[74:75], off nt
	global_load_dword v71, v[76:77], off nt
	global_load_dword v72, v[78:79], off nt
	global_load_dword v73, v[80:81], off nt
	s_nop 0
	global_load_dword v74, v[82:83], off nt
	global_load_dword v75, v[84:85], off nt
	s_branch .LBB0_10

; __device__ __forceinline__ float wave_sum(float v) { v = dpp_add16(v); return (rdlane(v, 0) + rdlane(v, 16)) + (rdlane(v, 32) + rdlane(v, 48)); }
; __device__ __forceinline__ void rms_row_to_both(const float* xrow, const float* g, bf16* orow, unsigned char* orow8, int lane) {
;     const f32x4* xr = (const f32x4*)xrow + lane; const f32x4* gr = (const f32x4*)g + lane;
;     f32x4 v[16]; float s = 0.f;
; #pragma unroll
;     for (int j = 0; j < 16; ++j) { v[j] = xr[64 * j]; s += (v[j].x * v[j].x + v[j].y * v[j].y) + (v[j].z * v[j].z + v[j].w * v[j].w); }
;     const float rs = 1.0f / sqrtf(wave_sum(s) * (1.f / D_) + 1e-6f);
.LBB0_49:
	global_load_dwordx4 v[26:29], v[96:97], off nt
	global_load_dwordx4 v[22:25], v[96:97], off offset:1024 nt
	global_load_dwordx4 v[54:57], v[96:97], off offset:2048 nt
	global_load_dwordx4 v[42:45], v[96:97], off offset:3072 nt
	v_add_co_u32_e32 v2, vcc, s3, v96
	s_add_i32 s29, s29, s34
	s_nop 0
	v_addc_co_u32_e32 v3, vcc, 0, v97, vcc
	v_add_co_u32_e32 v4, vcc, s8, v96
	s_cmpk_lt_i32 s29, 0x2000
	s_nop 0
	v_addc_co_u32_e32 v5, vcc, 0, v97, vcc
	v_add_co_u32_e32 v104, vcc, s9, v96
	s_waitcnt vmcnt(3)
	v_pk_mul_f32 v[106:107], v[26:27], v[26:27]
	v_addc_co_u32_e32 v105, vcc, 0, v97, vcc
	global_load_dwordx4 v[30:33], v[70:71], off
	global_load_dwordx4 v[66:69], v[4:5], off offset:-4096 nt
	global_load_dwordx4 v[50:53], v[2:3], off offset:3072 nt
	global_load_dwordx4 v[34:37], v[4:5], off offset:2048 nt
	global_load_dwordx4 v[10:13], v[104:105], off offset:1024 nt
	global_load_dwordx4 v[62:65], v[2:3], off offset:1024 nt
	global_load_dwordx4 v[58:61], v[2:3], off offset:2048 nt
	global_load_dwordx4 v[46:49], v[4:5], off nt
	global_load_dwordx4 v[38:41], v[4:5], off offset:1024 nt
	global_load_dwordx4 v[18:21], v[4:5], off offset:3072 nt
	global_load_dwordx4 v[14:17], v[104:105], off nt
	global_load_dwordx4 v[6:9], v[104:105], off offset:2048 nt
	s_nop 0
	global_load_dwordx4 v[2:5], v[104:105], off offset:3072 nt
	v_pk_mul_f32 v[104:105], v[28:29], v[28:29]
	s_waitcnt vmcnt(15)
	v_pk_mul_f32 v[108:109], v[24:25], v[24:25]
	v_pk_mul_f32 v[110:111], v[22:23], v[22:23]
	v_pk_mov_b32 v[114:115], v[106:107], v[104:105] op_sel:[1,0]
	v_mov_b32_e32 v107, v105
	v_pk_mov_b32 v[104:105], v[110:111], v[108:109] op_sel:[1,0]
	v_mov_b32_e32 v111, v109
	s_waitcnt vmcnt(14)
	v_mul_f32_e32 v100, v55, v55
	v_mul_f32_e32 v112, v57, v57
	v_pk_add_f32 v[106:107], v[114:115], v[106:107]
	v_pk_add_f32 v[104:105], v[104:105], v[110:111]
	s_waitcnt vmcnt(13)
	v_mul_f32_e32 v103, v44, v44
	v_mul_f32_e32 v133, v45, v45
	v_mul_f32_e32 v145, v42, v42
	v_mul_f32_e32 v146, v43, v43
	v_pk_fma_f32 v[130:131], v[54:55], v[54:55], v[100:101] op_sel_hi:[1,1,0]
	v_pk_fma_f32 v[112:113], v[56:57], v[56:57], v[112:113] op_sel_hi:[1,1,0]
	v_pk_add_f32 v[106:107], v[106:107], v[106:107] op_sel:[0,1] op_sel_hi:[1,0]
	v_pk_add_f32 v[104:105], v[104:105], v[104:105] op_sel:[0,1] op_sel_hi:[1,0]
	v_mov_b32_e32 v131, v103
	v_mov_b32_e32 v113, v133
	v_mov_b32_e32 v107, v145
	v_mov_b32_e32 v105, v146
	v_pk_add_f32 v[112:113], v[130:131], v[112:113]
	v_pk_add_f32 v[104:105], v[106:107], v[104:105]
	v_lshl_add_u64 v[96:97], v[96:97], 0, s[4:5]
	v_pk_add_f32 v[104:105], v[104:105], v[112:113]
	s_waitcnt vmcnt(11)
	v_pk_mul_f32 v[108:109], v[68:69], v[68:69]
	v_pk_mul_f32 v[116:117], v[66:67], v[66:67]
	s_waitcnt vmcnt(10)
	v_pk_mul_f32 v[118:119], v[52:53], v[52:53]
	v_pk_mov_b32 v[110:111], v[116:117], v[108:109] op_sel:[1,0]
	v_mov_b32_e32 v117, v109
	v_pk_mul_f32 v[120:121], v[50:51], v[50:51]
	s_waitcnt vmcnt(9)
	v_pk_mul_f32 v[122:123], v[36:37], v[36:37]
	v_pk_mul_f32 v[124:125], v[34:35], v[34:35]
	s_waitcnt vmcnt(8)
	v_pk_mul_f32 v[126:127], v[12:13], v[12:13]
	v_pk_mul_f32 v[128:129], v[10:11], v[10:11]
	s_waitcnt vmcnt(7)
	v_mul_f32_e32 v100, v63, v63
	v_mul_f32_e32 v132, v65, v65
	v_pk_add_f32 v[110:111], v[110:111], v[116:117]
	s_waitcnt vmcnt(6)
	v_mul_f32_e32 v147, v60, v60
	v_mul_f32_e32 v148, v61, v61
	v_mul_f32_e32 v155, v59, v59
	v_mul_f32_e32 v156, v58, v58
	v_pk_mov_b32 v[108:109], v[120:121], v[118:119] op_sel:[1,0]
	v_mov_b32_e32 v121, v119
	v_pk_mov_b32 v[114:115], v[124:125], v[122:123] op_sel:[1,0]
	v_mov_b32_e32 v125, v123
	v_pk_mov_b32 v[118:119], v[128:129], v[126:127] op_sel:[1,0]
	v_mov_b32_e32 v129, v127
	v_pk_fma_f32 v[122:123], v[62:63], v[62:63], v[100:101] op_sel_hi:[1,1,0]
	v_pk_fma_f32 v[126:127], v[64:65], v[64:65], v[132:133] op_sel_hi:[1,1,0]
	v_pk_add_f32 v[110:111], v[110:111], v[110:111] op_sel:[0,1] op_sel_hi:[1,0]
	v_pk_add_f32 v[104:105], v[104:105], v[104:105] op_sel:[0,1] op_sel_hi:[1,0]
	v_mov_b32_e32 v123, v147
	v_mov_b32_e32 v127, v148
	v_mov_b32_e32 v111, v155
	v_mov_b32_e32 v105, v156
	v_pk_add_f32 v[116:117], v[118:119], v[128:129]
	v_pk_add_f32 v[118:119], v[122:123], v[126:127]
	v_pk_add_f32 v[104:105], v[104:105], v[110:111]
	s_waitcnt vmcnt(5)
	v_mul_f32_e32 v134, v47, v47
	v_mul_f32_e32 v136, v49, v49
	v_pk_add_f32 v[108:109], v[108:109], v[120:121]
	v_pk_add_f32 v[104:105], v[104:105], v[118:119]
	s_waitcnt vmcnt(4)
	v_mul_f32_e32 v149, v40, v40
	v_mul_f32_e32 v150, v41, v41
	v_mul_f32_e32 v157, v39, v39
	v_mul_f32_e32 v158, v38, v38
	v_pk_fma_f32 v[132:133], v[46:47], v[46:47], v[134:135] op_sel_hi:[1,1,0]
	v_pk_fma_f32 v[134:135], v[48:49], v[48:49], v[136:137] op_sel_hi:[1,1,0]
	v_pk_add_f32 v[108:109], v[108:109], v[108:109] op_sel:[0,1] op_sel_hi:[1,0]
	v_pk_add_f32 v[104:105], v[104:105], v[104:105] op_sel:[0,1] op_sel_hi:[1,0]
	v_mov_b32_e32 v133, v149
	v_mov_b32_e32 v135, v150
	v_mov_b32_e32 v109, v157
	v_mov_b32_e32 v105, v158
	v_pk_add_f32 v[120:121], v[132:133], v[134:135]
	v_pk_add_f32 v[104:105], v[104:105], v[108:109]
	s_waitcnt vmcnt(3)
	v_mul_f32_e32 v138, v19, v19
	v_mul_f32_e32 v140, v21, v21
	v_pk_add_f32 v[114:115], v[114:115], v[124:125]
	v_pk_add_f32 v[104:105], v[104:105], v[120:121]
	s_waitcnt vmcnt(2)
	v_mul_f32_e32 v151, v16, v16
	v_mul_f32_e32 v152, v17, v17
	v_mul_f32_e32 v159, v15, v15
	v_mul_f32_e32 v160, v14, v14
	v_pk_fma_f32 v[136:137], v[18:19], v[18:19], v[138:139] op_sel_hi:[1,1,0]
	v_pk_fma_f32 v[138:139], v[20:21], v[20:21], v[140:141] op_sel_hi:[1,1,0]
	v_pk_add_f32 v[114:115], v[114:115], v[114:115] op_sel:[0,1] op_sel_hi:[1,0]
	v_pk_add_f32 v[104:105], v[104:105], v[104:105] op_sel:[0,1] op_sel_hi:[1,0]
	v_mov_b32_e32 v137, v151
	v_mov_b32_e32 v139, v152
	v_mov_b32_e32 v115, v159
	v_mov_b32_e32 v105, v160
	v_pk_add_f32 v[122:123], v[136:137], v[138:139]
	v_pk_add_f32 v[104:105], v[104:105], v[114:115]
	s_waitcnt vmcnt(1)
; __device__ __forceinline__ float rdlane(float v, int l) { return __builtin_bit_cast(float, __builtin_amdgcn_readlane(__builtin_bit_cast(int, v), l)); }
; __device__ __forceinline__ float wave_sum(float v) { v = dpp_add16(v); return (rdlane(v, 0) + rdlane(v, 16)) + (rdlane(v, 32) + rdlane(v, 48)); }
; __device__ __forceinline__ void rms_row_to_both(const float* xrow, const float* g, bf16* orow, unsigned char* orow8, int lane) {
;     ...
;     const float rs = 1.0f / sqrtf(wave_sum(s) * (1.f / D_) + 1e-6f);
;     unsigned* o4 = (unsigned*)orow8 + lane; (void)orow;
; #pragma unroll
;     for (int j = 0; j < 16; ++j) { const f32x4 y = v[j] * rs * gr[64 * j]; o4[64 * j] = pk4_i8(y.x * I8_SA, y.y * I8_SA, y.z * I8_SA, y.w * I8_SA); }
	v_mul_f32_e32 v142, v7, v7
	v_mul_f32_e32 v144, v9, v9
	v_pk_add_f32 v[104:105], v[104:105], v[122:123]
	s_waitcnt vmcnt(0)
	v_mul_f32_e32 v153, v4, v4
	v_mul_f32_e32 v154, v5, v5
	v_mul_f32_e32 v161, v3, v3
	v_mul_f32_e32 v162, v2, v2
	v_pk_fma_f32 v[140:141], v[6:7], v[6:7], v[142:143] op_sel_hi:[1,1,0]
	v_pk_fma_f32 v[142:143], v[8:9], v[8:9], v[144:145] op_sel_hi:[1,1,0]
	v_pk_add_f32 v[116:117], v[116:117], v[116:117] op_sel:[0,1] op_sel_hi:[1,0]
	v_pk_add_f32 v[104:105], v[104:105], v[104:105] op_sel:[0,1] op_sel_hi:[1,0]
	v_mov_b32_e32 v141, v153
	v_mov_b32_e32 v143, v154
	v_mov_b32_e32 v117, v161
	v_mov_b32_e32 v105, v162
	v_pk_add_f32 v[124:125], v[140:141], v[142:143]
	v_pk_add_f32 v[104:105], v[104:105], v[116:117]
	s_nop 0
	v_pk_add_f32 v[104:105], v[104:105], v[124:125]
	s_nop 0
	v_add_f32_e32 v100, v104, v105
	s_nop 1
	v_add_f32_dpp v100, v100, v100 quad_perm:[1,0,3,2] row_mask:0xf bank_mask:0xf bound_ctrl:1
	s_nop 1
	v_add_f32_dpp v100, v100, v100 quad_perm:[2,3,0,1] row_mask:0xf bank_mask:0xf bound_ctrl:1
	s_nop 1
	v_add_f32_dpp v100, v100, v100 row_half_mirror row_mask:0xf bank_mask:0xf bound_ctrl:1
	s_nop 1
	v_add_f32_dpp v100, v100, v100 row_mirror row_mask:0xf bank_mask:0xf bound_ctrl:1
	s_nop 0
	v_readlane_b32 s30, v100, 16
	v_readlane_b32 s31, v100, 48
	v_readlane_b32 s0, v100, 0
	v_readlane_b32 s1, v100, 32
	v_mov_b32_e32 v104, s30
	v_mov_b32_e32 v105, s31
	v_pk_add_f32 v[104:105], s[0:1], v[104:105]
	s_nop 0
	v_add_f32_e32 v100, v104, v105
	v_fmamk_f32 v100, v100, 0x39800000, v1
	v_mul_f32_e32 v103, 0x4f800000, v100
	v_cmp_gt_f32_e32 vcc, s10, v100
	s_nop 1
	v_cndmask_b32_e32 v100, v100, v103, vcc
	v_sqrt_f32_e32 v103, v100
	s_nop 0
	v_add_u32_e32 v104, -1, v103
	v_add_u32_e32 v105, 1, v103
	v_fma_f32 v106, -v104, v103, v100
	v_fma_f32 v107, -v105, v103, v100
	v_cmp_ge_f32_e64 s[0:1], 0, v106
	s_nop 1
	v_cndmask_b32_e64 v103, v103, v104, s[0:1]
	v_cmp_lt_f32_e64 s[0:1], 0, v107
	s_nop 1
	v_cndmask_b32_e64 v103, v103, v105, s[0:1]
	v_mul_f32_e32 v104, 0x37800000, v103
	v_cndmask_b32_e32 v103, v103, v104, vcc
	v_cmp_class_f32_e32 vcc, v100, v101
	s_nop 1
	v_cndmask_b32_e32 v100, v103, v100, vcc
	v_div_scale_f32 v103, s[0:1], v100, v100, 1.0
	v_rcp_f32_e32 v105, v103
	v_div_scale_f32 v104, vcc, 1.0, v100, 1.0
	v_fma_f32 v106, -v103, v105, 1.0
	v_fmac_f32_e32 v105, v106, v105
	v_mul_f32_e32 v106, v104, v105
	v_fma_f32 v107, -v103, v106, v104
	v_fmac_f32_e32 v106, v107, v105
	v_fma_f32 v103, -v103, v106, v104
	v_div_fmas_f32 v103, v103, v105, v106
	v_div_fixup_f32 v100, v103, v100, 1.0
	v_pk_mul_f32 v[26:27], v[26:27], v[100:101] op_sel_hi:[1,0]
	v_pk_mul_f32 v[28:29], v[28:29], v[100:101] op_sel_hi:[1,0]
	v_pk_mul_f32 v[26:27], v[30:31], v[26:27]
	v_pk_mul_f32 v[28:29], v[32:33], v[28:29]
	v_mul_f32_e32 v27, 0x41c80000, v27
	v_mul_f32_e32 v26, 0x41c80000, v26
	v_mul_f32_e32 v28, 0x41c80000, v28
	v_mul_f32_e32 v29, 0x41c80000, v29
	v_med3_f32 v27, v27, s11, v102
	v_med3_f32 v26, v26, s11, v102
	v_med3_f32 v29, v29, s11, v102
	v_med3_f32 v28, v28, s11, v102
	v_rndne_f32_e32 v27, v27
	v_rndne_f32_e32 v26, v26
	v_rndne_f32_e32 v29, v29
	v_rndne_f32_e32 v28, v28
	v_cvt_i32_f32_e32 v27, v27
	v_cvt_i32_f32_e32 v26, v26
	v_cvt_i32_f32_e32 v29, v29
	v_cvt_i32_f32_sdwa v28, v28 dst_sel:WORD_1 dst_unused:UNUSED_PAD src0_sel:DWORD
	v_lshlrev_b32_e32 v27, 8, v27
	v_and_b32_e32 v27, 0xff00, v27
	v_perm_b32 v26, v29, v26, s28
	v_and_b32_e32 v28, 0xff0000, v28
	v_or3_b32 v26, v26, v27, v28
	global_store_dword v[98:99], v26, off
	v_mov_b64_e32 v[26:27], v[164:165]
	v_mov_b64_e32 v[28:29], v[166:167]
	v_pk_mul_f32 v[22:23], v[22:23], v[100:101] op_sel_hi:[1,0]
	v_pk_mul_f32 v[24:25], v[24:25], v[100:101] op_sel_hi:[1,0]
	v_pk_mul_f32 v[54:55], v[54:55], v[100:101] op_sel_hi:[1,0]
	v_pk_mul_f32 v[56:57], v[56:57], v[100:101] op_sel_hi:[1,0]
	v_pk_mul_f32 v[42:43], v[42:43], v[100:101] op_sel_hi:[1,0]
	v_pk_mul_f32 v[44:45], v[44:45], v[100:101] op_sel_hi:[1,0]
	v_pk_mul_f32 v[66:67], v[66:67], v[100:101] op_sel_hi:[1,0]
	v_pk_mul_f32 v[68:69], v[68:69], v[100:101] op_sel_hi:[1,0]
	v_pk_mul_f32 v[62:63], v[62:63], v[100:101] op_sel_hi:[1,0]
	v_pk_mul_f32 v[64:65], v[64:65], v[100:101] op_sel_hi:[1,0]
	v_pk_mul_f32 v[58:59], v[58:59], v[100:101] op_sel_hi:[1,0]
	v_pk_mul_f32 v[60:61], v[60:61], v[100:101] op_sel_hi:[1,0]
	v_pk_mul_f32 v[50:51], v[50:51], v[100:101] op_sel_hi:[1,0]
	v_pk_mul_f32 v[52:53], v[52:53], v[100:101] op_sel_hi:[1,0]
	v_pk_mul_f32 v[46:47], v[46:47], v[100:101] op_sel_hi:[1,0]
	v_pk_mul_f32 v[48:49], v[48:49], v[100:101] op_sel_hi:[1,0]
	v_pk_mul_f32 v[38:39], v[38:39], v[100:101] op_sel_hi:[1,0]
	v_pk_mul_f32 v[40:41], v[40:41], v[100:101] op_sel_hi:[1,0]
	v_pk_mul_f32 v[34:35], v[34:35], v[100:101] op_sel_hi:[1,0]
	v_pk_mul_f32 v[36:37], v[36:37], v[100:101] op_sel_hi:[1,0]
	v_pk_mul_f32 v[18:19], v[18:19], v[100:101] op_sel_hi:[1,0]
	v_pk_mul_f32 v[20:21], v[20:21], v[100:101] op_sel_hi:[1,0]
	v_pk_mul_f32 v[14:15], v[14:15], v[100:101] op_sel_hi:[1,0]
	v_pk_mul_f32 v[16:17], v[16:17], v[100:101] op_sel_hi:[1,0]
	v_pk_mul_f32 v[10:11], v[10:11], v[100:101] op_sel_hi:[1,0]
	v_pk_mul_f32 v[12:13], v[12:13], v[100:101] op_sel_hi:[1,0]
	v_pk_mul_f32 v[6:7], v[6:7], v[100:101] op_sel_hi:[1,0]
	v_pk_mul_f32 v[8:9], v[8:9], v[100:101] op_sel_hi:[1,0]
	v_pk_mul_f32 v[2:3], v[2:3], v[100:101] op_sel_hi:[1,0]
	v_pk_mul_f32 v[4:5], v[4:5], v[100:101] op_sel_hi:[1,0]
	v_pk_mul_f32 v[22:23], v[26:27], v[22:23]
	v_pk_mul_f32 v[24:25], v[28:29], v[24:25]
	v_mul_f32_e32 v23, 0x41c80000, v23
	v_mul_f32_e32 v22, 0x41c80000, v22
	v_mul_f32_e32 v24, 0x41c80000, v24
	v_mul_f32_e32 v25, 0x41c80000, v25
	v_med3_f32 v23, v23, s11, v102
; __device__ __forceinline__ void rms_row_to_both(const float* xrow, const float* g, bf16* orow, unsigned char* orow8, int lane) {
;     ...
; #pragma unroll
;     for (int j = 0; j < 16; ++j) { const f32x4 y = v[j] * rs * gr[64 * j]; o4[64 * j] = pk4_i8(y.x * I8_SA, y.y * I8_SA, y.z * I8_SA, y.w * I8_SA); }
	v_med3_f32 v22, v22, s11, v102
	v_med3_f32 v25, v25, s11, v102
	v_med3_f32 v24, v24, s11, v102
	v_rndne_f32_e32 v23, v23
	v_rndne_f32_e32 v22, v22
	v_rndne_f32_e32 v25, v25
	v_rndne_f32_e32 v24, v24
	v_cvt_i32_f32_e32 v23, v23
	v_cvt_i32_f32_e32 v22, v22
	v_cvt_i32_f32_e32 v25, v25
	v_cvt_i32_f32_sdwa v24, v24 dst_sel:WORD_1 dst_unused:UNUSED_PAD src0_sel:DWORD
	v_lshlrev_b32_e32 v23, 8, v23
	v_and_b32_e32 v23, 0xff00, v23
	v_perm_b32 v22, v25, v22, s28
	v_and_b32_e32 v24, 0xff0000, v24
	v_or3_b32 v22, v22, v23, v24
	global_store_dword v[98:99], v22, off offset:256
	v_mov_b64_e32 v[22:23], v[168:169]
	v_mov_b64_e32 v[24:25], v[170:171]
	v_pk_mul_f32 v[22:23], v[22:23], v[54:55]
	v_pk_mul_f32 v[24:25], v[24:25], v[56:57]
	v_mul_f32_e32 v23, 0x41c80000, v23
	v_mul_f32_e32 v22, 0x41c80000, v22
	v_mul_f32_e32 v24, 0x41c80000, v24
	v_mul_f32_e32 v25, 0x41c80000, v25
	v_med3_f32 v23, v23, s11, v102
	v_med3_f32 v22, v22, s11, v102
	v_med3_f32 v24, v24, s11, v102
	v_med3_f32 v25, v25, s11, v102
	v_rndne_f32_e32 v23, v23
	v_rndne_f32_e32 v22, v22
	v_rndne_f32_e32 v24, v24
	v_rndne_f32_e32 v25, v25
	v_cvt_i32_f32_e32 v23, v23
	v_cvt_i32_f32_e32 v22, v22
	v_cvt_i32_f32_sdwa v24, v24 dst_sel:WORD_1 dst_unused:UNUSED_PAD src0_sel:DWORD
	v_cvt_i32_f32_e32 v25, v25
	v_lshlrev_b32_e32 v23, 8, v23
	v_and_b32_e32 v23, 0xff00, v23
	v_and_b32_e32 v24, 0xff0000, v24
	v_perm_b32 v22, v25, v22, s28
	v_or3_b32 v22, v22, v23, v24
	global_store_dword v[98:99], v22, off offset:512
	v_mov_b64_e32 v[22:23], v[172:173]
	v_mov_b64_e32 v[24:25], v[174:175]
	v_pk_mul_f32 v[22:23], v[22:23], v[42:43]
	v_pk_mul_f32 v[24:25], v[24:25], v[44:45]
	v_mul_f32_e32 v23, 0x41c80000, v23
	v_mul_f32_e32 v22, 0x41c80000, v22
	v_mul_f32_e32 v24, 0x41c80000, v24
	v_mul_f32_e32 v25, 0x41c80000, v25
	v_med3_f32 v23, v23, s11, v102
	v_med3_f32 v22, v22, s11, v102
	v_med3_f32 v24, v24, s11, v102
	v_med3_f32 v25, v25, s11, v102
	v_rndne_f32_e32 v23, v23
	v_rndne_f32_e32 v22, v22
	v_rndne_f32_e32 v24, v24
	v_rndne_f32_e32 v25, v25
	v_cvt_i32_f32_e32 v23, v23
	v_cvt_i32_f32_e32 v22, v22
	v_cvt_i32_f32_sdwa v24, v24 dst_sel:WORD_1 dst_unused:UNUSED_PAD src0_sel:DWORD
	v_cvt_i32_f32_e32 v25, v25
	v_lshlrev_b32_e32 v23, 8, v23
	v_and_b32_e32 v23, 0xff00, v23
	v_and_b32_e32 v24, 0xff0000, v24
	v_perm_b32 v22, v25, v22, s28
	v_or3_b32 v22, v22, v23, v24
	global_store_dword v[98:99], v22, off offset:768
	v_mov_b64_e32 v[22:23], v[176:177]
	v_mov_b64_e32 v[24:25], v[178:179]
	v_pk_mul_f32 v[22:23], v[66:67], v[22:23]
	v_pk_mul_f32 v[24:25], v[68:69], v[24:25]
	v_mul_f32_e32 v23, 0x41c80000, v23
	v_mul_f32_e32 v22, 0x41c80000, v22
	v_mul_f32_e32 v24, 0x41c80000, v24
	v_mul_f32_e32 v25, 0x41c80000, v25
	v_med3_f32 v23, v23, s11, v102
	v_med3_f32 v22, v22, s11, v102
	v_med3_f32 v24, v24, s11, v102
	v_med3_f32 v25, v25, s11, v102
	v_rndne_f32_e32 v23, v23
	v_rndne_f32_e32 v22, v22
	v_rndne_f32_e32 v24, v24
	v_rndne_f32_e32 v25, v25
	v_cvt_i32_f32_e32 v23, v23
	v_cvt_i32_f32_e32 v22, v22
	v_cvt_i32_f32_sdwa v24, v24 dst_sel:WORD_1 dst_unused:UNUSED_PAD src0_sel:DWORD
	v_cvt_i32_f32_e32 v25, v25
	v_lshlrev_b32_e32 v23, 8, v23
	v_and_b32_e32 v23, 0xff00, v23
	v_and_b32_e32 v24, 0xff0000, v24
	v_perm_b32 v22, v25, v22, s28
	v_or3_b32 v22, v22, v23, v24
	global_store_dword v[98:99], v22, off offset:1024
	v_mov_b64_e32 v[22:23], v[180:181]
	v_mov_b64_e32 v[24:25], v[182:183]
	v_pk_mul_f32 v[22:23], v[62:63], v[22:23]
	v_pk_mul_f32 v[24:25], v[64:65], v[24:25]
	v_mul_f32_e32 v23, 0x41c80000, v23
	v_mul_f32_e32 v22, 0x41c80000, v22
	v_mul_f32_e32 v24, 0x41c80000, v24
	v_mul_f32_e32 v25, 0x41c80000, v25
	v_med3_f32 v23, v23, s11, v102
	v_med3_f32 v22, v22, s11, v102
	v_med3_f32 v24, v24, s11, v102
	v_med3_f32 v25, v25, s11, v102
	v_rndne_f32_e32 v23, v23
	v_rndne_f32_e32 v22, v22
	v_rndne_f32_e32 v24, v24
	v_rndne_f32_e32 v25, v25
	v_cvt_i32_f32_e32 v23, v23
	v_cvt_i32_f32_e32 v22, v22
	v_cvt_i32_f32_sdwa v24, v24 dst_sel:WORD_1 dst_unused:UNUSED_PAD src0_sel:DWORD
	v_cvt_i32_f32_e32 v25, v25
	v_lshlrev_b32_e32 v23, 8, v23
	v_and_b32_e32 v23, 0xff00, v23
	v_and_b32_e32 v24, 0xff0000, v24
	v_perm_b32 v22, v25, v22, s28
	v_or3_b32 v22, v22, v23, v24
	global_store_dword v[98:99], v22, off offset:1280
	v_mov_b64_e32 v[22:23], v[184:185]
	v_mov_b64_e32 v[24:25], v[186:187]
	v_pk_mul_f32 v[22:23], v[58:59], v[22:23]
	v_pk_mul_f32 v[24:25], v[60:61], v[24:25]
	v_mul_f32_e32 v23, 0x41c80000, v23
	v_mul_f32_e32 v22, 0x41c80000, v22
	v_mul_f32_e32 v24, 0x41c80000, v24
	v_mul_f32_e32 v25, 0x41c80000, v25
	v_med3_f32 v23, v23, s11, v102
	v_med3_f32 v22, v22, s11, v102
	v_med3_f32 v24, v24, s11, v102
	v_med3_f32 v25, v25, s11, v102
	v_rndne_f32_e32 v23, v23
	v_rndne_f32_e32 v22, v22
	v_rndne_f32_e32 v24, v24
	v_rndne_f32_e32 v25, v25
	v_cvt_i32_f32_e32 v23, v23
	v_cvt_i32_f32_e32 v22, v22
	v_cvt_i32_f32_sdwa v24, v24 dst_sel:WORD_1 dst_unused:UNUSED_PAD src0_sel:DWORD
	v_cvt_i32_f32_e32 v25, v25
	v_lshlrev_b32_e32 v23, 8, v23
	v_and_b32_e32 v23, 0xff00, v23
	v_and_b32_e32 v24, 0xff0000, v24
	v_perm_b32 v22, v25, v22, s28
	v_or3_b32 v22, v22, v23, v24
	global_store_dword v[98:99], v22, off offset:1536
	v_mov_b64_e32 v[22:23], v[188:189]
	v_mov_b64_e32 v[24:25], v[190:191]
	v_pk_mul_f32 v[22:23], v[50:51], v[22:23]
	v_pk_mul_f32 v[24:25], v[52:53], v[24:25]
	v_mul_f32_e32 v23, 0x41c80000, v23
	v_mul_f32_e32 v22, 0x41c80000, v22
	v_mul_f32_e32 v24, 0x41c80000, v24
	v_mul_f32_e32 v25, 0x41c80000, v25
	v_med3_f32 v23, v23, s11, v102
	v_med3_f32 v22, v22, s11, v102
	v_med3_f32 v24, v24, s11, v102
	v_med3_f32 v25, v25, s11, v102
	v_rndne_f32_e32 v23, v23
	v_rndne_f32_e32 v22, v22
	v_rndne_f32_e32 v24, v24
	v_rndne_f32_e32 v25, v25
; __device__ __forceinline__ void rms_row_to_both(const float* xrow, const float* g, bf16* orow, unsigned char* orow8, int lane) {
;     ...
; #pragma unroll
;     for (int j = 0; j < 16; ++j) { const f32x4 y = v[j] * rs * gr[64 * j]; o4[64 * j] = pk4_i8(y.x * I8_SA, y.y * I8_SA, y.z * I8_SA, y.w * I8_SA); }
	v_cvt_i32_f32_e32 v23, v23
	v_cvt_i32_f32_e32 v22, v22
	v_cvt_i32_f32_sdwa v24, v24 dst_sel:WORD_1 dst_unused:UNUSED_PAD src0_sel:DWORD
	v_cvt_i32_f32_e32 v25, v25
	v_lshlrev_b32_e32 v23, 8, v23
	v_and_b32_e32 v23, 0xff00, v23
	v_and_b32_e32 v24, 0xff0000, v24
	v_perm_b32 v22, v25, v22, s28
	v_or3_b32 v22, v22, v23, v24
	global_store_dword v[98:99], v22, off offset:1792
	v_mov_b64_e32 v[22:23], v[192:193]
	v_mov_b64_e32 v[24:25], v[194:195]
	v_pk_mul_f32 v[22:23], v[46:47], v[22:23]
	v_pk_mul_f32 v[24:25], v[48:49], v[24:25]
	v_mul_f32_e32 v23, 0x41c80000, v23
	v_mul_f32_e32 v22, 0x41c80000, v22
	v_mul_f32_e32 v24, 0x41c80000, v24
	v_mul_f32_e32 v25, 0x41c80000, v25
	v_med3_f32 v23, v23, s11, v102
	v_med3_f32 v22, v22, s11, v102
	v_med3_f32 v24, v24, s11, v102
	v_med3_f32 v25, v25, s11, v102
	v_rndne_f32_e32 v23, v23
	v_rndne_f32_e32 v22, v22
	v_rndne_f32_e32 v24, v24
	v_rndne_f32_e32 v25, v25
	v_cvt_i32_f32_e32 v23, v23
	v_cvt_i32_f32_e32 v22, v22
	v_cvt_i32_f32_sdwa v24, v24 dst_sel:WORD_1 dst_unused:UNUSED_PAD src0_sel:DWORD
	v_cvt_i32_f32_e32 v25, v25
	v_lshlrev_b32_e32 v23, 8, v23
	v_and_b32_e32 v23, 0xff00, v23
	v_and_b32_e32 v24, 0xff0000, v24
	v_perm_b32 v22, v25, v22, s28
	v_or3_b32 v22, v22, v23, v24
	global_store_dword v[98:99], v22, off offset:2048
	v_mov_b64_e32 v[22:23], v[196:197]
	v_mov_b64_e32 v[24:25], v[198:199]
	v_pk_mul_f32 v[22:23], v[38:39], v[22:23]
	v_pk_mul_f32 v[24:25], v[40:41], v[24:25]
	v_mul_f32_e32 v23, 0x41c80000, v23
	v_mul_f32_e32 v22, 0x41c80000, v22
	v_mul_f32_e32 v24, 0x41c80000, v24
	v_mul_f32_e32 v25, 0x41c80000, v25
	v_med3_f32 v23, v23, s11, v102
	v_med3_f32 v22, v22, s11, v102
	v_med3_f32 v24, v24, s11, v102
	v_med3_f32 v25, v25, s11, v102
	v_rndne_f32_e32 v23, v23
	v_rndne_f32_e32 v22, v22
	v_rndne_f32_e32 v24, v24
	v_rndne_f32_e32 v25, v25
	v_cvt_i32_f32_e32 v23, v23
	v_cvt_i32_f32_e32 v22, v22
	v_cvt_i32_f32_sdwa v24, v24 dst_sel:WORD_1 dst_unused:UNUSED_PAD src0_sel:DWORD
	v_cvt_i32_f32_e32 v25, v25
	v_lshlrev_b32_e32 v23, 8, v23
	v_and_b32_e32 v23, 0xff00, v23
	v_and_b32_e32 v24, 0xff0000, v24
	v_perm_b32 v22, v25, v22, s28
	v_or3_b32 v22, v22, v23, v24
	global_store_dword v[98:99], v22, off offset:2304
	v_mov_b64_e32 v[22:23], v[200:201]
	v_mov_b64_e32 v[24:25], v[202:203]
	v_pk_mul_f32 v[22:23], v[34:35], v[22:23]
	v_pk_mul_f32 v[24:25], v[36:37], v[24:25]
	v_mul_f32_e32 v23, 0x41c80000, v23
	v_mul_f32_e32 v22, 0x41c80000, v22
	v_mul_f32_e32 v24, 0x41c80000, v24
	v_mul_f32_e32 v25, 0x41c80000, v25
	v_med3_f32 v23, v23, s11, v102
	v_med3_f32 v22, v22, s11, v102
	v_med3_f32 v24, v24, s11, v102
	v_med3_f32 v25, v25, s11, v102
	v_rndne_f32_e32 v23, v23
	v_rndne_f32_e32 v22, v22
	v_rndne_f32_e32 v24, v24
	v_rndne_f32_e32 v25, v25
	v_cvt_i32_f32_e32 v23, v23
	v_cvt_i32_f32_e32 v22, v22
	v_cvt_i32_f32_sdwa v24, v24 dst_sel:WORD_1 dst_unused:UNUSED_PAD src0_sel:DWORD
	v_cvt_i32_f32_e32 v25, v25
	v_lshlrev_b32_e32 v23, 8, v23
	v_and_b32_e32 v23, 0xff00, v23
	v_and_b32_e32 v24, 0xff0000, v24
	v_perm_b32 v22, v25, v22, s28
	v_or3_b32 v22, v22, v23, v24
	global_store_dword v[98:99], v22, off offset:2560
	v_mov_b64_e32 v[22:23], v[204:205]
	v_mov_b64_e32 v[24:25], v[206:207]
	v_pk_mul_f32 v[18:19], v[18:19], v[22:23]
	v_pk_mul_f32 v[20:21], v[20:21], v[24:25]
	v_mul_f32_e32 v19, 0x41c80000, v19
	v_mul_f32_e32 v18, 0x41c80000, v18
	v_mul_f32_e32 v20, 0x41c80000, v20
	v_mul_f32_e32 v21, 0x41c80000, v21
	v_med3_f32 v19, v19, s11, v102
	v_med3_f32 v18, v18, s11, v102
	v_med3_f32 v20, v20, s11, v102
	v_med3_f32 v21, v21, s11, v102
	v_rndne_f32_e32 v19, v19
	v_rndne_f32_e32 v18, v18
	v_rndne_f32_e32 v20, v20
	v_rndne_f32_e32 v21, v21
	v_cvt_i32_f32_e32 v19, v19
	v_cvt_i32_f32_e32 v18, v18
	v_cvt_i32_f32_sdwa v20, v20 dst_sel:WORD_1 dst_unused:UNUSED_PAD src0_sel:DWORD
	v_cvt_i32_f32_e32 v21, v21
; __device__ __forceinline__ void rms_row_to_both(const float* xrow, const float* g, bf16* orow, unsigned char* orow8, int lane) {
;     ...
; #pragma unroll
;     for (int j = 0; j < 16; ++j) { const f32x4 y = v[j] * rs * gr[64 * j]; o4[64 * j] = pk4_i8(y.x * I8_SA, y.y * I8_SA, y.z * I8_SA, y.w * I8_SA); }
	v_lshlrev_b32_e32 v19, 8, v19
	v_and_b32_e32 v19, 0xff00, v19
	v_and_b32_e32 v20, 0xff0000, v20
	v_perm_b32 v18, v21, v18, s28
	v_or3_b32 v18, v18, v19, v20
	global_store_dword v[98:99], v18, off offset:2816
	v_mov_b64_e32 v[18:19], v[208:209]
	v_mov_b64_e32 v[20:21], v[210:211]
	v_pk_mul_f32 v[14:15], v[14:15], v[18:19]
	v_pk_mul_f32 v[16:17], v[16:17], v[20:21]
	v_mul_f32_e32 v15, 0x41c80000, v15
	v_mul_f32_e32 v14, 0x41c80000, v14
	v_mul_f32_e32 v16, 0x41c80000, v16
	v_mul_f32_e32 v17, 0x41c80000, v17
	v_med3_f32 v15, v15, s11, v102
	v_med3_f32 v14, v14, s11, v102
	v_med3_f32 v16, v16, s11, v102
	v_med3_f32 v17, v17, s11, v102
	v_rndne_f32_e32 v15, v15
	v_rndne_f32_e32 v14, v14
	v_rndne_f32_e32 v16, v16
	v_rndne_f32_e32 v17, v17
	v_cvt_i32_f32_e32 v15, v15
	v_cvt_i32_f32_e32 v14, v14
	v_cvt_i32_f32_sdwa v16, v16 dst_sel:WORD_1 dst_unused:UNUSED_PAD src0_sel:DWORD
	v_cvt_i32_f32_e32 v17, v17
	v_lshlrev_b32_e32 v15, 8, v15
	v_and_b32_e32 v15, 0xff00, v15
	v_and_b32_e32 v16, 0xff0000, v16
	v_perm_b32 v14, v17, v14, s28
	v_or3_b32 v14, v14, v15, v16
	global_store_dword v[98:99], v14, off offset:3072
	v_mov_b64_e32 v[14:15], v[212:213]
	v_mov_b64_e32 v[16:17], v[214:215]
	v_pk_mul_f32 v[10:11], v[10:11], v[14:15]
	v_pk_mul_f32 v[12:13], v[12:13], v[16:17]
	v_mul_f32_e32 v11, 0x41c80000, v11
	v_mul_f32_e32 v10, 0x41c80000, v10
	v_mul_f32_e32 v12, 0x41c80000, v12
	v_mul_f32_e32 v13, 0x41c80000, v13
	v_med3_f32 v11, v11, s11, v102
	v_med3_f32 v10, v10, s11, v102
	v_med3_f32 v12, v12, s11, v102
	v_med3_f32 v13, v13, s11, v102
	v_rndne_f32_e32 v11, v11
	v_rndne_f32_e32 v10, v10
	v_rndne_f32_e32 v12, v12
	v_rndne_f32_e32 v13, v13
	v_cvt_i32_f32_e32 v11, v11
	v_cvt_i32_f32_e32 v10, v10
	v_cvt_i32_f32_sdwa v12, v12 dst_sel:WORD_1 dst_unused:UNUSED_PAD src0_sel:DWORD
	v_cvt_i32_f32_e32 v13, v13
	v_lshlrev_b32_e32 v11, 8, v11
	v_and_b32_e32 v11, 0xff00, v11
	v_and_b32_e32 v12, 0xff0000, v12
	v_perm_b32 v10, v13, v10, s28
	v_or3_b32 v10, v10, v11, v12
	global_store_dword v[98:99], v10, off offset:3328
	v_mov_b64_e32 v[10:11], v[216:217]
	v_mov_b64_e32 v[12:13], v[218:219]
	v_pk_mul_f32 v[6:7], v[6:7], v[10:11]
	v_pk_mul_f32 v[8:9], v[8:9], v[12:13]
	v_mul_f32_e32 v7, 0x41c80000, v7
	v_mul_f32_e32 v6, 0x41c80000, v6
	v_mul_f32_e32 v8, 0x41c80000, v8
	v_mul_f32_e32 v9, 0x41c80000, v9
	v_med3_f32 v7, v7, s11, v102
	v_med3_f32 v6, v6, s11, v102
	v_med3_f32 v8, v8, s11, v102
	v_med3_f32 v9, v9, s11, v102
	v_rndne_f32_e32 v7, v7
	v_rndne_f32_e32 v6, v6
	v_rndne_f32_e32 v8, v8
	v_rndne_f32_e32 v9, v9
	v_cvt_i32_f32_e32 v7, v7
	v_cvt_i32_f32_e32 v6, v6
	v_cvt_i32_f32_sdwa v8, v8 dst_sel:WORD_1 dst_unused:UNUSED_PAD src0_sel:DWORD
	v_cvt_i32_f32_e32 v9, v9
	v_lshlrev_b32_e32 v7, 8, v7
	v_and_b32_e32 v7, 0xff00, v7
	v_and_b32_e32 v8, 0xff0000, v8
	v_perm_b32 v6, v9, v6, s28
	v_or3_b32 v6, v6, v7, v8
	global_store_dword v[98:99], v6, off offset:3584
	v_mov_b64_e32 v[6:7], v[220:221]
	v_mov_b64_e32 v[8:9], v[222:223]
	v_pk_mul_f32 v[2:3], v[2:3], v[6:7]
	v_pk_mul_f32 v[4:5], v[4:5], v[8:9]
	v_mul_f32_e32 v3, 0x41c80000, v3
	v_mul_f32_e32 v2, 0x41c80000, v2
	v_mul_f32_e32 v4, 0x41c80000, v4
	v_mul_f32_e32 v5, 0x41c80000, v5
	v_med3_f32 v3, v3, s11, v102
	v_med3_f32 v2, v2, s11, v102
	v_med3_f32 v4, v4, s11, v102
	v_med3_f32 v5, v5, s11, v102
	v_rndne_f32_e32 v3, v3
	v_rndne_f32_e32 v2, v2
	v_rndne_f32_e32 v4, v4
	v_rndne_f32_e32 v5, v5
	v_cvt_i32_f32_e32 v3, v3
	v_cvt_i32_f32_e32 v2, v2
	v_cvt_i32_f32_sdwa v4, v4 dst_sel:WORD_1 dst_unused:UNUSED_PAD src0_sel:DWORD
	v_cvt_i32_f32_e32 v5, v5
	v_lshlrev_b32_e32 v3, 8, v3
	v_and_b32_e32 v3, 0xff00, v3
	v_and_b32_e32 v4, 0xff0000, v4
	v_perm_b32 v2, v5, v2, s28
	v_or3_b32 v2, v2, v3, v4
	global_store_dword v[98:99], v2, off offset:3840
	v_lshl_add_u64 v[98:99], v[98:99], 0, s[6:7]
	s_cbranch_scc1 .LBB0_49
	s_mov_b32 s95, s33
